# P7 epilogue: transcendentals interleaved with independent clamp/add ops instead of bursts of 8
# baseline (speedup 1.0000x reference)
.Lp7_nopf:
	v_mov_b32_e32 v176, 0x41000000
	v_mov_b32_e32 v178, 0xc01d265f
	v_mov_b32_e32 v150, s5
	ds_read_b32 v151, v150
	v_or_b32_e32 v150, s66, v159
	s_waitcnt vmcnt(12)
	s_waitcnt lgkmcnt(0)
	v_subrev_u32_e32 v151, s8, v151
	v_cmp_lt_i32_e32 vcc, v150, v151
	s_and_saveexec_b64 s[0:1], vcc
	s_cbranch_execz .LBB0_967
	v_mul_f32_e32 v174, 0x3a800000, v158
	v_cvt_f32_i32_e32 v138, v138
	v_cvt_f32_i32_e32 v139, v139
	v_cvt_f32_i32_e32 v140, v140
	v_cvt_f32_i32_e32 v141, v141
	v_cvt_f32_i32_e32 v134, v134
	v_cvt_f32_i32_e32 v135, v135
	v_cvt_f32_i32_e32 v136, v136
	v_cvt_f32_i32_e32 v137, v137
	v_cvt_f32_i32_e32 v122, v122
	v_cvt_f32_i32_e32 v123, v123
	v_cvt_f32_i32_e32 v124, v124
	v_cvt_f32_i32_e32 v125, v125
	v_cvt_f32_i32_e32 v118, v118
	v_cvt_f32_i32_e32 v119, v119
	v_cvt_f32_i32_e32 v120, v120
	v_cvt_f32_i32_e32 v121, v121
	v_pk_fma_f32 v[138:139], v[138:139], v[174:175], v[146:147] op_sel_hi:[1,0,1]
	v_pk_fma_f32 v[134:135], v[134:135], v[174:175], v[142:143] op_sel_hi:[1,0,1]
	v_pk_fma_f32 v[140:141], v[140:141], v[174:175], v[148:149] op_sel_hi:[1,0,1]
	v_pk_fma_f32 v[136:137], v[136:137], v[174:175], v[144:145] op_sel_hi:[1,0,1]
	v_pk_fma_f32 v[122:123], v[122:123], v[174:175], v[130:131] op_sel_hi:[1,0,1]
	v_pk_fma_f32 v[118:119], v[118:119], v[174:175], v[126:127] op_sel_hi:[1,0,1]
	v_pk_fma_f32 v[124:125], v[124:125], v[174:175], v[132:133] op_sel_hi:[1,0,1]
	v_pk_fma_f32 v[120:121], v[120:121], v[174:175], v[128:129] op_sel_hi:[1,0,1]
	v_min_f32_e32 v138, 0x40e00000, v138
	v_min_f32_e32 v139, 0x40e00000, v139
	v_min_f32_e32 v140, 0x40e00000, v140
	v_min_f32_e32 v141, 0x40e00000, v141
	v_min_f32_e32 v122, 0x40e00000, v122
	v_min_f32_e32 v123, 0x40e00000, v123
	v_min_f32_e32 v124, 0x40e00000, v124
	v_min_f32_e32 v125, 0x40e00000, v125
	v_pk_mul_f32 v[166:167], v[138:139], v[178:179] op_sel_hi:[1,0]
	v_pk_mul_f32 v[168:169], v[140:141], v[178:179] op_sel_hi:[1,0]
	v_pk_mul_f32 v[170:171], v[122:123], v[178:179] op_sel_hi:[1,0]
	v_pk_mul_f32 v[172:173], v[124:125], v[178:179] op_sel_hi:[1,0]
	v_exp_f32_e32 v166, v166
	v_med3_f32 v134, v134, s74, v223
	v_exp_f32_e32 v167, v167
	v_med3_f32 v135, v135, s74, v223
	v_exp_f32_e32 v168, v168
	v_med3_f32 v136, v136, s74, v223
	v_exp_f32_e32 v169, v169
	v_med3_f32 v137, v137, s74, v223
	v_exp_f32_e32 v170, v170
	v_med3_f32 v118, v118, s74, v223
	v_exp_f32_e32 v171, v171
	v_med3_f32 v119, v119, s74, v223
	v_exp_f32_e32 v172, v172
	v_med3_f32 v120, v120, s74, v223
	v_exp_f32_e32 v173, v173
	v_med3_f32 v121, v121, s74, v223
	v_pk_add_f32 v[166:167], v[166:167], 1.0 op_sel_hi:[1,0]
	v_pk_add_f32 v[168:169], v[168:169], 1.0 op_sel_hi:[1,0]
	v_pk_add_f32 v[170:171], v[170:171], 1.0 op_sel_hi:[1,0]
	v_pk_add_f32 v[172:173], v[172:173], 1.0 op_sel_hi:[1,0]
	v_rcp_f32_e32 v166, v166
	v_rcp_f32_e32 v167, v167
	v_pk_add_f32 v[134:135], v[134:135], 1.0 op_sel_hi:[1,0]
	v_rcp_f32_e32 v168, v168
	v_rcp_f32_e32 v169, v169
	v_pk_add_f32 v[136:137], v[136:137], 1.0 op_sel_hi:[1,0]
	v_rcp_f32_e32 v170, v170
	v_rcp_f32_e32 v171, v171
	v_pk_add_f32 v[118:119], v[118:119], 1.0 op_sel_hi:[1,0]
	v_rcp_f32_e32 v172, v172
	v_rcp_f32_e32 v173, v173
	v_pk_add_f32 v[120:121], v[120:121], 1.0 op_sel_hi:[1,0]
	s_nop 0
	v_pk_mul_f32 v[138:139], v[138:139], v[166:167]
	v_pk_mul_f32 v[140:141], v[140:141], v[168:169]
	v_pk_mul_f32 v[122:123], v[122:123], v[170:171]
	v_pk_mul_f32 v[124:125], v[124:125], v[172:173]
	v_pk_mul_f32 v[134:135], v[134:135], v[138:139]
	v_pk_mul_f32 v[136:137], v[136:137], v[140:141]
	v_pk_mul_f32 v[118:119], v[118:119], v[122:123]
	v_pk_mul_f32 v[120:121], v[120:121], v[124:125]
	v_pk_fma_f32 v[134:135], v[134:135], v[176:177], v[222:223] op_sel_hi:[1,0,0]
	v_pk_fma_f32 v[136:137], v[136:137], v[176:177], v[222:223] op_sel_hi:[1,0,0]
	v_pk_fma_f32 v[118:119], v[118:119], v[176:177], v[222:223] op_sel_hi:[1,0,0]
	v_pk_fma_f32 v[120:121], v[120:121], v[176:177], v[222:223] op_sel_hi:[1,0,0]
	v_med3_f32 v134, v134, s75, v224
	v_med3_f32 v135, v135, s75, v224
	v_med3_f32 v136, v136, s75, v224
	v_med3_f32 v137, v137, s75, v224
	v_med3_f32 v118, v118, s75, v224
	v_med3_f32 v119, v119, s75, v224
	v_med3_f32 v120, v120, s75, v224
	v_med3_f32 v121, v121, s75, v224
	v_perm_b32 v134, v135, v134, s76
	v_perm_b32 v136, v137, v136, s76
	v_perm_b32 v118, v119, v118, s76
	v_perm_b32 v120, v121, v120, s76
	v_perm_b32 v166, v136, v134, s77
	v_perm_b32 v167, v120, v118, s77
	v_add_u32_e32 v118, s4, v150
	v_ashrrev_i32_e32 v119, 31, v118
	v_lshlrev_b64 v[118:119], 11, v[118:119]
	v_lshl_add_u64 v[118:119], s[10:11], 0, v[118:119]
	v_lshl_add_u64 v[118:119], v[118:119], 0, v[4:5]
	v_mov_b32_e32 v134, v166
	v_mov_b32_e32 v135, v167
	global_store_dwordx2 v[118:119], v[134:135], off
.LBB0_967:
	s_or_b64 exec, exec, s[0:1]
	v_or_b32_e32 v118, 16, v150
	v_cmp_lt_i32_e32 vcc, v118, v151
	s_and_saveexec_b64 s[0:1], vcc
	s_cbranch_execz .LBB0_969
	v_mul_f32_e32 v174, 0x3a800000, v157
	v_cvt_f32_i32_e32 v114, v114
	v_cvt_f32_i32_e32 v115, v115
	v_cvt_f32_i32_e32 v116, v116
	v_cvt_f32_i32_e32 v117, v117
	v_cvt_f32_i32_e32 v110, v110
	v_cvt_f32_i32_e32 v111, v111
	v_cvt_f32_i32_e32 v112, v112
	v_cvt_f32_i32_e32 v113, v113
	v_cvt_f32_i32_e32 v106, v106
	v_cvt_f32_i32_e32 v107, v107
	v_cvt_f32_i32_e32 v108, v108
	v_cvt_f32_i32_e32 v109, v109
	v_cvt_f32_i32_e32 v102, v102
	v_cvt_f32_i32_e32 v103, v103
	v_cvt_f32_i32_e32 v104, v104
	v_cvt_f32_i32_e32 v105, v105
	v_pk_fma_f32 v[114:115], v[114:115], v[174:175], v[146:147] op_sel_hi:[1,0,1]
	v_pk_fma_f32 v[110:111], v[110:111], v[174:175], v[142:143] op_sel_hi:[1,0,1]
	v_pk_fma_f32 v[116:117], v[116:117], v[174:175], v[148:149] op_sel_hi:[1,0,1]
	v_pk_fma_f32 v[112:113], v[112:113], v[174:175], v[144:145] op_sel_hi:[1,0,1]
	v_pk_fma_f32 v[106:107], v[106:107], v[174:175], v[130:131] op_sel_hi:[1,0,1]
	v_pk_fma_f32 v[102:103], v[102:103], v[174:175], v[126:127] op_sel_hi:[1,0,1]
	v_pk_fma_f32 v[108:109], v[108:109], v[174:175], v[132:133] op_sel_hi:[1,0,1]
	v_pk_fma_f32 v[104:105], v[104:105], v[174:175], v[128:129] op_sel_hi:[1,0,1]
	v_min_f32_e32 v114, 0x40e00000, v114
	v_min_f32_e32 v115, 0x40e00000, v115
	v_min_f32_e32 v116, 0x40e00000, v116
	v_min_f32_e32 v117, 0x40e00000, v117
	v_min_f32_e32 v106, 0x40e00000, v106
	v_min_f32_e32 v107, 0x40e00000, v107
	v_min_f32_e32 v108, 0x40e00000, v108
	v_min_f32_e32 v109, 0x40e00000, v109
	v_pk_mul_f32 v[166:167], v[114:115], v[178:179] op_sel_hi:[1,0]
	v_pk_mul_f32 v[168:169], v[116:117], v[178:179] op_sel_hi:[1,0]
	v_pk_mul_f32 v[170:171], v[106:107], v[178:179] op_sel_hi:[1,0]
	v_pk_mul_f32 v[172:173], v[108:109], v[178:179] op_sel_hi:[1,0]
	v_exp_f32_e32 v166, v166
	v_med3_f32 v110, v110, s74, v223
	v_exp_f32_e32 v167, v167
	v_med3_f32 v111, v111, s74, v223
	v_exp_f32_e32 v168, v168
	v_med3_f32 v112, v112, s74, v223
	v_exp_f32_e32 v169, v169
	v_med3_f32 v113, v113, s74, v223
	v_exp_f32_e32 v170, v170
	v_med3_f32 v102, v102, s74, v223
	v_exp_f32_e32 v171, v171
	v_med3_f32 v103, v103, s74, v223
	v_exp_f32_e32 v172, v172
	v_med3_f32 v104, v104, s74, v223
	v_exp_f32_e32 v173, v173
	v_med3_f32 v105, v105, s74, v223
	v_pk_add_f32 v[166:167], v[166:167], 1.0 op_sel_hi:[1,0]
	v_pk_add_f32 v[168:169], v[168:169], 1.0 op_sel_hi:[1,0]
	v_pk_add_f32 v[170:171], v[170:171], 1.0 op_sel_hi:[1,0]
	v_pk_add_f32 v[172:173], v[172:173], 1.0 op_sel_hi:[1,0]
	v_rcp_f32_e32 v166, v166
	v_rcp_f32_e32 v167, v167
	v_pk_add_f32 v[110:111], v[110:111], 1.0 op_sel_hi:[1,0]
	v_rcp_f32_e32 v168, v168
	v_rcp_f32_e32 v169, v169
	v_pk_add_f32 v[112:113], v[112:113], 1.0 op_sel_hi:[1,0]
	v_rcp_f32_e32 v170, v170
	v_rcp_f32_e32 v171, v171
	v_pk_add_f32 v[102:103], v[102:103], 1.0 op_sel_hi:[1,0]
	v_rcp_f32_e32 v172, v172
	v_rcp_f32_e32 v173, v173
	v_pk_add_f32 v[104:105], v[104:105], 1.0 op_sel_hi:[1,0]
	s_nop 0
	v_pk_mul_f32 v[114:115], v[114:115], v[166:167]
	v_pk_mul_f32 v[116:117], v[116:117], v[168:169]
	v_pk_mul_f32 v[106:107], v[106:107], v[170:171]
	v_pk_mul_f32 v[108:109], v[108:109], v[172:173]
	v_pk_mul_f32 v[110:111], v[110:111], v[114:115]
	v_pk_mul_f32 v[112:113], v[112:113], v[116:117]
	v_pk_mul_f32 v[102:103], v[102:103], v[106:107]
	v_pk_mul_f32 v[104:105], v[104:105], v[108:109]
	v_pk_fma_f32 v[110:111], v[110:111], v[176:177], v[222:223] op_sel_hi:[1,0,0]
	v_pk_fma_f32 v[112:113], v[112:113], v[176:177], v[222:223] op_sel_hi:[1,0,0]
	v_pk_fma_f32 v[102:103], v[102:103], v[176:177], v[222:223] op_sel_hi:[1,0,0]
	v_pk_fma_f32 v[104:105], v[104:105], v[176:177], v[222:223] op_sel_hi:[1,0,0]
	v_med3_f32 v110, v110, s75, v224
	v_med3_f32 v111, v111, s75, v224
	v_med3_f32 v112, v112, s75, v224
	v_med3_f32 v113, v113, s75, v224
	v_med3_f32 v102, v102, s75, v224
	v_med3_f32 v103, v103, s75, v224
	v_med3_f32 v104, v104, s75, v224
	v_med3_f32 v105, v105, s75, v224
	v_perm_b32 v110, v111, v110, s76
	v_perm_b32 v112, v113, v112, s76
	v_perm_b32 v102, v103, v102, s76
	v_perm_b32 v104, v105, v104, s76
	v_perm_b32 v166, v112, v110, s77
	v_perm_b32 v167, v104, v102, s77
	v_add_u32_e32 v102, s4, v118
	v_ashrrev_i32_e32 v103, 31, v102
	v_lshlrev_b64 v[102:103], 11, v[102:103]
	v_lshl_add_u64 v[102:103], s[10:11], 0, v[102:103]
	v_lshl_add_u64 v[102:103], v[102:103], 0, v[4:5]
	v_mov_b32_e32 v110, v166
	v_mov_b32_e32 v111, v167
	global_store_dwordx2 v[102:103], v[110:111], off
.LBB0_969:
	s_or_b64 exec, exec, s[0:1]
	v_or_b32_e32 v102, 32, v150
	v_cmp_lt_i32_e32 vcc, v102, v151
	s_and_saveexec_b64 s[0:1], vcc
	s_cbranch_execz .LBB0_971
	v_mul_f32_e32 v174, 0x3a800000, v156
	v_cvt_f32_i32_e32 v98, v98
	v_cvt_f32_i32_e32 v99, v99
	v_cvt_f32_i32_e32 v100, v100
	v_cvt_f32_i32_e32 v101, v101
	v_cvt_f32_i32_e32 v94, v94
	v_cvt_f32_i32_e32 v95, v95
	v_cvt_f32_i32_e32 v96, v96
	v_cvt_f32_i32_e32 v97, v97
	v_cvt_f32_i32_e32 v90, v90
	v_cvt_f32_i32_e32 v91, v91
	v_cvt_f32_i32_e32 v92, v92
	v_cvt_f32_i32_e32 v93, v93
	v_cvt_f32_i32_e32 v86, v86
	v_cvt_f32_i32_e32 v87, v87
	v_cvt_f32_i32_e32 v88, v88
	v_cvt_f32_i32_e32 v89, v89
	v_pk_fma_f32 v[98:99], v[98:99], v[174:175], v[146:147] op_sel_hi:[1,0,1]
	v_pk_fma_f32 v[94:95], v[94:95], v[174:175], v[142:143] op_sel_hi:[1,0,1]
	v_pk_fma_f32 v[100:101], v[100:101], v[174:175], v[148:149] op_sel_hi:[1,0,1]
	v_pk_fma_f32 v[96:97], v[96:97], v[174:175], v[144:145] op_sel_hi:[1,0,1]
	v_pk_fma_f32 v[90:91], v[90:91], v[174:175], v[130:131] op_sel_hi:[1,0,1]
	v_pk_fma_f32 v[86:87], v[86:87], v[174:175], v[126:127] op_sel_hi:[1,0,1]
	v_pk_fma_f32 v[92:93], v[92:93], v[174:175], v[132:133] op_sel_hi:[1,0,1]
	v_pk_fma_f32 v[88:89], v[88:89], v[174:175], v[128:129] op_sel_hi:[1,0,1]
	v_min_f32_e32 v98, 0x40e00000, v98
	v_min_f32_e32 v99, 0x40e00000, v99
	v_min_f32_e32 v100, 0x40e00000, v100
	v_min_f32_e32 v101, 0x40e00000, v101
	v_min_f32_e32 v90, 0x40e00000, v90
	v_min_f32_e32 v91, 0x40e00000, v91
	v_min_f32_e32 v92, 0x40e00000, v92
	v_min_f32_e32 v93, 0x40e00000, v93
	v_pk_mul_f32 v[166:167], v[98:99], v[178:179] op_sel_hi:[1,0]
	v_pk_mul_f32 v[168:169], v[100:101], v[178:179] op_sel_hi:[1,0]
	v_pk_mul_f32 v[170:171], v[90:91], v[178:179] op_sel_hi:[1,0]
	v_pk_mul_f32 v[172:173], v[92:93], v[178:179] op_sel_hi:[1,0]
	v_exp_f32_e32 v166, v166
	v_med3_f32 v94, v94, s74, v223
	v_exp_f32_e32 v167, v167
	v_med3_f32 v95, v95, s74, v223
	v_exp_f32_e32 v168, v168
	v_med3_f32 v96, v96, s74, v223
	v_exp_f32_e32 v169, v169
	v_med3_f32 v97, v97, s74, v223
	v_exp_f32_e32 v170, v170
	v_med3_f32 v86, v86, s74, v223
	v_exp_f32_e32 v171, v171
	v_med3_f32 v87, v87, s74, v223
	v_exp_f32_e32 v172, v172
	v_med3_f32 v88, v88, s74, v223
	v_exp_f32_e32 v173, v173
	v_med3_f32 v89, v89, s74, v223
	v_pk_add_f32 v[166:167], v[166:167], 1.0 op_sel_hi:[1,0]
	v_pk_add_f32 v[168:169], v[168:169], 1.0 op_sel_hi:[1,0]
	v_pk_add_f32 v[170:171], v[170:171], 1.0 op_sel_hi:[1,0]
	v_pk_add_f32 v[172:173], v[172:173], 1.0 op_sel_hi:[1,0]
	v_rcp_f32_e32 v166, v166
	v_rcp_f32_e32 v167, v167
	v_pk_add_f32 v[94:95], v[94:95], 1.0 op_sel_hi:[1,0]
	v_rcp_f32_e32 v168, v168
	v_rcp_f32_e32 v169, v169
	v_pk_add_f32 v[96:97], v[96:97], 1.0 op_sel_hi:[1,0]
	v_rcp_f32_e32 v170, v170
	v_rcp_f32_e32 v171, v171
	v_pk_add_f32 v[86:87], v[86:87], 1.0 op_sel_hi:[1,0]
	v_rcp_f32_e32 v172, v172
	v_rcp_f32_e32 v173, v173
	v_pk_add_f32 v[88:89], v[88:89], 1.0 op_sel_hi:[1,0]
	s_nop 0
	v_pk_mul_f32 v[98:99], v[98:99], v[166:167]
	v_pk_mul_f32 v[100:101], v[100:101], v[168:169]
	v_pk_mul_f32 v[90:91], v[90:91], v[170:171]
	v_pk_mul_f32 v[92:93], v[92:93], v[172:173]
	v_pk_mul_f32 v[94:95], v[94:95], v[98:99]
	v_pk_mul_f32 v[96:97], v[96:97], v[100:101]
	v_pk_mul_f32 v[86:87], v[86:87], v[90:91]
	v_pk_mul_f32 v[88:89], v[88:89], v[92:93]
	v_pk_fma_f32 v[94:95], v[94:95], v[176:177], v[222:223] op_sel_hi:[1,0,0]
	v_pk_fma_f32 v[96:97], v[96:97], v[176:177], v[222:223] op_sel_hi:[1,0,0]
	v_pk_fma_f32 v[86:87], v[86:87], v[176:177], v[222:223] op_sel_hi:[1,0,0]
	v_pk_fma_f32 v[88:89], v[88:89], v[176:177], v[222:223] op_sel_hi:[1,0,0]
	v_med3_f32 v94, v94, s75, v224
	v_med3_f32 v95, v95, s75, v224
	v_med3_f32 v96, v96, s75, v224
	v_med3_f32 v97, v97, s75, v224
	v_med3_f32 v86, v86, s75, v224
	v_med3_f32 v87, v87, s75, v224
	v_med3_f32 v88, v88, s75, v224
	v_med3_f32 v89, v89, s75, v224
	v_perm_b32 v94, v95, v94, s76
	v_perm_b32 v96, v97, v96, s76
	v_perm_b32 v86, v87, v86, s76
	v_perm_b32 v88, v89, v88, s76
	v_perm_b32 v166, v96, v94, s77
	v_perm_b32 v167, v88, v86, s77
	v_add_u32_e32 v86, s4, v102
	v_ashrrev_i32_e32 v87, 31, v86
	v_lshlrev_b64 v[86:87], 11, v[86:87]
	v_lshl_add_u64 v[86:87], s[10:11], 0, v[86:87]
	v_lshl_add_u64 v[86:87], v[86:87], 0, v[4:5]
	v_mov_b32_e32 v94, v166
	v_mov_b32_e32 v95, v167
	global_store_dwordx2 v[86:87], v[94:95], off
.LBB0_971:
	s_or_b64 exec, exec, s[0:1]
	v_or_b32_e32 v86, 48, v150
	v_cmp_lt_i32_e32 vcc, v86, v151
	s_and_saveexec_b64 s[0:1], vcc
	s_cbranch_execz .LBB0_973
	v_mul_f32_e32 v174, 0x3a800000, v155
	v_cvt_f32_i32_e32 v82, v82
	v_cvt_f32_i32_e32 v83, v83
	v_cvt_f32_i32_e32 v84, v84
	v_cvt_f32_i32_e32 v85, v85
	v_cvt_f32_i32_e32 v78, v78
	v_cvt_f32_i32_e32 v79, v79
	v_cvt_f32_i32_e32 v80, v80
	v_cvt_f32_i32_e32 v81, v81
	v_cvt_f32_i32_e32 v74, v74
	v_cvt_f32_i32_e32 v75, v75
	v_cvt_f32_i32_e32 v76, v76
	v_cvt_f32_i32_e32 v77, v77
	v_cvt_f32_i32_e32 v70, v70
	v_cvt_f32_i32_e32 v71, v71
	v_cvt_f32_i32_e32 v72, v72
	v_cvt_f32_i32_e32 v73, v73
	v_pk_fma_f32 v[82:83], v[82:83], v[174:175], v[146:147] op_sel_hi:[1,0,1]
	v_pk_fma_f32 v[78:79], v[78:79], v[174:175], v[142:143] op_sel_hi:[1,0,1]
	v_pk_fma_f32 v[84:85], v[84:85], v[174:175], v[148:149] op_sel_hi:[1,0,1]
	v_pk_fma_f32 v[80:81], v[80:81], v[174:175], v[144:145] op_sel_hi:[1,0,1]
	v_pk_fma_f32 v[74:75], v[74:75], v[174:175], v[130:131] op_sel_hi:[1,0,1]
	v_pk_fma_f32 v[70:71], v[70:71], v[174:175], v[126:127] op_sel_hi:[1,0,1]
	v_pk_fma_f32 v[76:77], v[76:77], v[174:175], v[132:133] op_sel_hi:[1,0,1]
	v_pk_fma_f32 v[72:73], v[72:73], v[174:175], v[128:129] op_sel_hi:[1,0,1]
	v_min_f32_e32 v82, 0x40e00000, v82
	v_min_f32_e32 v83, 0x40e00000, v83
	v_min_f32_e32 v84, 0x40e00000, v84
	v_min_f32_e32 v85, 0x40e00000, v85
	v_min_f32_e32 v74, 0x40e00000, v74
	v_min_f32_e32 v75, 0x40e00000, v75
	v_min_f32_e32 v76, 0x40e00000, v76
	v_min_f32_e32 v77, 0x40e00000, v77
	v_pk_mul_f32 v[166:167], v[82:83], v[178:179] op_sel_hi:[1,0]
	v_pk_mul_f32 v[168:169], v[84:85], v[178:179] op_sel_hi:[1,0]
	v_pk_mul_f32 v[170:171], v[74:75], v[178:179] op_sel_hi:[1,0]
	v_pk_mul_f32 v[172:173], v[76:77], v[178:179] op_sel_hi:[1,0]
	v_exp_f32_e32 v166, v166
	v_med3_f32 v78, v78, s74, v223
	v_exp_f32_e32 v167, v167
	v_med3_f32 v79, v79, s74, v223
	v_exp_f32_e32 v168, v168
	v_med3_f32 v80, v80, s74, v223
	v_exp_f32_e32 v169, v169
	v_med3_f32 v81, v81, s74, v223
	v_exp_f32_e32 v170, v170
	v_med3_f32 v70, v70, s74, v223
	v_exp_f32_e32 v171, v171
	v_med3_f32 v71, v71, s74, v223
	v_exp_f32_e32 v172, v172
	v_med3_f32 v72, v72, s74, v223
	v_exp_f32_e32 v173, v173
	v_med3_f32 v73, v73, s74, v223
	v_pk_add_f32 v[166:167], v[166:167], 1.0 op_sel_hi:[1,0]
	v_pk_add_f32 v[168:169], v[168:169], 1.0 op_sel_hi:[1,0]
	v_pk_add_f32 v[170:171], v[170:171], 1.0 op_sel_hi:[1,0]
	v_pk_add_f32 v[172:173], v[172:173], 1.0 op_sel_hi:[1,0]
	v_rcp_f32_e32 v166, v166
	v_rcp_f32_e32 v167, v167
	v_pk_add_f32 v[78:79], v[78:79], 1.0 op_sel_hi:[1,0]
	v_rcp_f32_e32 v168, v168
	v_rcp_f32_e32 v169, v169
	v_pk_add_f32 v[80:81], v[80:81], 1.0 op_sel_hi:[1,0]
	v_rcp_f32_e32 v170, v170
	v_rcp_f32_e32 v171, v171
	v_pk_add_f32 v[70:71], v[70:71], 1.0 op_sel_hi:[1,0]
	v_rcp_f32_e32 v172, v172
	v_rcp_f32_e32 v173, v173
	v_pk_add_f32 v[72:73], v[72:73], 1.0 op_sel_hi:[1,0]
	s_nop 0
	v_pk_mul_f32 v[82:83], v[82:83], v[166:167]
	v_pk_mul_f32 v[84:85], v[84:85], v[168:169]
	v_pk_mul_f32 v[74:75], v[74:75], v[170:171]
	v_pk_mul_f32 v[76:77], v[76:77], v[172:173]
	v_pk_mul_f32 v[78:79], v[78:79], v[82:83]
	v_pk_mul_f32 v[80:81], v[80:81], v[84:85]
	v_pk_mul_f32 v[70:71], v[70:71], v[74:75]
	v_pk_mul_f32 v[72:73], v[72:73], v[76:77]
	v_pk_fma_f32 v[78:79], v[78:79], v[176:177], v[222:223] op_sel_hi:[1,0,0]
	v_pk_fma_f32 v[80:81], v[80:81], v[176:177], v[222:223] op_sel_hi:[1,0,0]
	v_pk_fma_f32 v[70:71], v[70:71], v[176:177], v[222:223] op_sel_hi:[1,0,0]
	v_pk_fma_f32 v[72:73], v[72:73], v[176:177], v[222:223] op_sel_hi:[1,0,0]
	v_med3_f32 v78, v78, s75, v224
	v_med3_f32 v79, v79, s75, v224
	v_med3_f32 v80, v80, s75, v224
	v_med3_f32 v81, v81, s75, v224
	v_med3_f32 v70, v70, s75, v224
	v_med3_f32 v71, v71, s75, v224
	v_med3_f32 v72, v72, s75, v224
	v_med3_f32 v73, v73, s75, v224
	v_perm_b32 v78, v79, v78, s76
	v_perm_b32 v80, v81, v80, s76
	v_perm_b32 v70, v71, v70, s76
	v_perm_b32 v72, v73, v72, s76
	v_perm_b32 v166, v80, v78, s77
	v_perm_b32 v167, v72, v70, s77
	v_add_u32_e32 v70, s4, v86
	v_ashrrev_i32_e32 v71, 31, v70
	v_lshlrev_b64 v[70:71], 11, v[70:71]
	v_lshl_add_u64 v[70:71], s[10:11], 0, v[70:71]
	v_lshl_add_u64 v[70:71], v[70:71], 0, v[4:5]
	v_mov_b32_e32 v78, v166
	v_mov_b32_e32 v79, v167
	global_store_dwordx2 v[70:71], v[78:79], off
.LBB0_973:
	s_or_b64 exec, exec, s[0:1]
	v_add_u32_e32 v70, 0x80, v150
	v_cmp_lt_i32_e32 vcc, v70, v151
	s_and_saveexec_b64 s[0:1], vcc
	s_cbranch_execz .LBB0_975
	v_mul_f32_e32 v174, 0x3a800000, v154
	v_cvt_f32_i32_e32 v66, v66
	v_cvt_f32_i32_e32 v67, v67
	v_cvt_f32_i32_e32 v68, v68
	v_cvt_f32_i32_e32 v69, v69
	v_cvt_f32_i32_e32 v62, v62
	v_cvt_f32_i32_e32 v63, v63
	v_cvt_f32_i32_e32 v64, v64
	v_cvt_f32_i32_e32 v65, v65
	v_cvt_f32_i32_e32 v58, v58
	v_cvt_f32_i32_e32 v59, v59
	v_cvt_f32_i32_e32 v60, v60
	v_cvt_f32_i32_e32 v61, v61
	v_cvt_f32_i32_e32 v54, v54
	v_cvt_f32_i32_e32 v55, v55
	v_cvt_f32_i32_e32 v56, v56
	v_cvt_f32_i32_e32 v57, v57
	v_pk_fma_f32 v[66:67], v[66:67], v[174:175], v[146:147] op_sel_hi:[1,0,1]
	v_pk_fma_f32 v[62:63], v[62:63], v[174:175], v[142:143] op_sel_hi:[1,0,1]
	v_pk_fma_f32 v[68:69], v[68:69], v[174:175], v[148:149] op_sel_hi:[1,0,1]
	v_pk_fma_f32 v[64:65], v[64:65], v[174:175], v[144:145] op_sel_hi:[1,0,1]
	v_pk_fma_f32 v[58:59], v[58:59], v[174:175], v[130:131] op_sel_hi:[1,0,1]
	v_pk_fma_f32 v[54:55], v[54:55], v[174:175], v[126:127] op_sel_hi:[1,0,1]
	v_pk_fma_f32 v[60:61], v[60:61], v[174:175], v[132:133] op_sel_hi:[1,0,1]
	v_pk_fma_f32 v[56:57], v[56:57], v[174:175], v[128:129] op_sel_hi:[1,0,1]
	v_min_f32_e32 v66, 0x40e00000, v66
	v_min_f32_e32 v67, 0x40e00000, v67
	v_min_f32_e32 v68, 0x40e00000, v68
	v_min_f32_e32 v69, 0x40e00000, v69
	v_min_f32_e32 v58, 0x40e00000, v58
	v_min_f32_e32 v59, 0x40e00000, v59
	v_min_f32_e32 v60, 0x40e00000, v60
	v_min_f32_e32 v61, 0x40e00000, v61
	v_pk_mul_f32 v[166:167], v[66:67], v[178:179] op_sel_hi:[1,0]
	v_pk_mul_f32 v[168:169], v[68:69], v[178:179] op_sel_hi:[1,0]
	v_pk_mul_f32 v[170:171], v[58:59], v[178:179] op_sel_hi:[1,0]
	v_pk_mul_f32 v[172:173], v[60:61], v[178:179] op_sel_hi:[1,0]
	v_exp_f32_e32 v166, v166
	v_med3_f32 v62, v62, s74, v223
	v_exp_f32_e32 v167, v167
	v_med3_f32 v63, v63, s74, v223
	v_exp_f32_e32 v168, v168
	v_med3_f32 v64, v64, s74, v223
	v_exp_f32_e32 v169, v169
	v_med3_f32 v65, v65, s74, v223
	v_exp_f32_e32 v170, v170
	v_med3_f32 v54, v54, s74, v223
	v_exp_f32_e32 v171, v171
	v_med3_f32 v55, v55, s74, v223
	v_exp_f32_e32 v172, v172
	v_med3_f32 v56, v56, s74, v223
	v_exp_f32_e32 v173, v173
	v_med3_f32 v57, v57, s74, v223
	v_pk_add_f32 v[166:167], v[166:167], 1.0 op_sel_hi:[1,0]
	v_pk_add_f32 v[168:169], v[168:169], 1.0 op_sel_hi:[1,0]
	v_pk_add_f32 v[170:171], v[170:171], 1.0 op_sel_hi:[1,0]
	v_pk_add_f32 v[172:173], v[172:173], 1.0 op_sel_hi:[1,0]
	v_rcp_f32_e32 v166, v166
	v_rcp_f32_e32 v167, v167
	v_pk_add_f32 v[62:63], v[62:63], 1.0 op_sel_hi:[1,0]
	v_rcp_f32_e32 v168, v168
	v_rcp_f32_e32 v169, v169
	v_pk_add_f32 v[64:65], v[64:65], 1.0 op_sel_hi:[1,0]
	v_rcp_f32_e32 v170, v170
	v_rcp_f32_e32 v171, v171
	v_pk_add_f32 v[54:55], v[54:55], 1.0 op_sel_hi:[1,0]
	v_rcp_f32_e32 v172, v172
	v_rcp_f32_e32 v173, v173
	v_pk_add_f32 v[56:57], v[56:57], 1.0 op_sel_hi:[1,0]
	s_nop 0
	v_pk_mul_f32 v[66:67], v[66:67], v[166:167]
	v_pk_mul_f32 v[68:69], v[68:69], v[168:169]
	v_pk_mul_f32 v[58:59], v[58:59], v[170:171]
	v_pk_mul_f32 v[60:61], v[60:61], v[172:173]
	v_pk_mul_f32 v[62:63], v[62:63], v[66:67]
	v_pk_mul_f32 v[64:65], v[64:65], v[68:69]
	v_pk_mul_f32 v[54:55], v[54:55], v[58:59]
	v_pk_mul_f32 v[56:57], v[56:57], v[60:61]
	v_pk_fma_f32 v[62:63], v[62:63], v[176:177], v[222:223] op_sel_hi:[1,0,0]
	v_pk_fma_f32 v[64:65], v[64:65], v[176:177], v[222:223] op_sel_hi:[1,0,0]
	v_pk_fma_f32 v[54:55], v[54:55], v[176:177], v[222:223] op_sel_hi:[1,0,0]
	v_pk_fma_f32 v[56:57], v[56:57], v[176:177], v[222:223] op_sel_hi:[1,0,0]
	v_med3_f32 v62, v62, s75, v224
	v_med3_f32 v63, v63, s75, v224
	v_med3_f32 v64, v64, s75, v224
	v_med3_f32 v65, v65, s75, v224
	v_med3_f32 v54, v54, s75, v224
	v_med3_f32 v55, v55, s75, v224
	v_med3_f32 v56, v56, s75, v224
	v_med3_f32 v57, v57, s75, v224
	v_perm_b32 v62, v63, v62, s76
	v_perm_b32 v64, v65, v64, s76
	v_perm_b32 v54, v55, v54, s76
	v_perm_b32 v56, v57, v56, s76
	v_perm_b32 v166, v64, v62, s77
	v_perm_b32 v167, v56, v54, s77
	v_add_u32_e32 v54, s4, v70
	v_ashrrev_i32_e32 v55, 31, v54
	v_lshlrev_b64 v[54:55], 11, v[54:55]
	v_lshl_add_u64 v[54:55], s[10:11], 0, v[54:55]
	v_lshl_add_u64 v[54:55], v[54:55], 0, v[4:5]
	v_mov_b32_e32 v62, v166
	v_mov_b32_e32 v63, v167
	global_store_dwordx2 v[54:55], v[62:63], off
.LBB0_975:
	s_or_b64 exec, exec, s[0:1]
	v_add_u32_e32 v54, 0x90, v150
	v_cmp_lt_i32_e32 vcc, v54, v151
	s_and_saveexec_b64 s[0:1], vcc
	s_cbranch_execz .LBB0_977
	v_mul_f32_e32 v174, 0x3a800000, v153
	v_cvt_f32_i32_e32 v50, v50
	v_cvt_f32_i32_e32 v51, v51
	v_cvt_f32_i32_e32 v52, v52
	v_cvt_f32_i32_e32 v53, v53
	v_cvt_f32_i32_e32 v46, v46
	v_cvt_f32_i32_e32 v47, v47
	v_cvt_f32_i32_e32 v48, v48
	v_cvt_f32_i32_e32 v49, v49
	v_cvt_f32_i32_e32 v42, v42
	v_cvt_f32_i32_e32 v43, v43
	v_cvt_f32_i32_e32 v44, v44
	v_cvt_f32_i32_e32 v45, v45
	v_cvt_f32_i32_e32 v38, v38
	v_cvt_f32_i32_e32 v39, v39
	v_cvt_f32_i32_e32 v40, v40
	v_cvt_f32_i32_e32 v41, v41
	v_pk_fma_f32 v[50:51], v[50:51], v[174:175], v[146:147] op_sel_hi:[1,0,1]
	v_pk_fma_f32 v[46:47], v[46:47], v[174:175], v[142:143] op_sel_hi:[1,0,1]
	v_pk_fma_f32 v[52:53], v[52:53], v[174:175], v[148:149] op_sel_hi:[1,0,1]
	v_pk_fma_f32 v[48:49], v[48:49], v[174:175], v[144:145] op_sel_hi:[1,0,1]
	v_pk_fma_f32 v[42:43], v[42:43], v[174:175], v[130:131] op_sel_hi:[1,0,1]
	v_pk_fma_f32 v[38:39], v[38:39], v[174:175], v[126:127] op_sel_hi:[1,0,1]
	v_pk_fma_f32 v[44:45], v[44:45], v[174:175], v[132:133] op_sel_hi:[1,0,1]
	v_pk_fma_f32 v[40:41], v[40:41], v[174:175], v[128:129] op_sel_hi:[1,0,1]
	v_min_f32_e32 v50, 0x40e00000, v50
	v_min_f32_e32 v51, 0x40e00000, v51
	v_min_f32_e32 v52, 0x40e00000, v52
	v_min_f32_e32 v53, 0x40e00000, v53
	v_min_f32_e32 v42, 0x40e00000, v42
	v_min_f32_e32 v43, 0x40e00000, v43
	v_min_f32_e32 v44, 0x40e00000, v44
	v_min_f32_e32 v45, 0x40e00000, v45
	v_pk_mul_f32 v[166:167], v[50:51], v[178:179] op_sel_hi:[1,0]
	v_pk_mul_f32 v[168:169], v[52:53], v[178:179] op_sel_hi:[1,0]
	v_pk_mul_f32 v[170:171], v[42:43], v[178:179] op_sel_hi:[1,0]
	v_pk_mul_f32 v[172:173], v[44:45], v[178:179] op_sel_hi:[1,0]
	v_exp_f32_e32 v166, v166
	v_med3_f32 v46, v46, s74, v223
	v_exp_f32_e32 v167, v167
	v_med3_f32 v47, v47, s74, v223
	v_exp_f32_e32 v168, v168
	v_med3_f32 v48, v48, s74, v223
	v_exp_f32_e32 v169, v169
	v_med3_f32 v49, v49, s74, v223
	v_exp_f32_e32 v170, v170
	v_med3_f32 v38, v38, s74, v223
	v_exp_f32_e32 v171, v171
	v_med3_f32 v39, v39, s74, v223
	v_exp_f32_e32 v172, v172
	v_med3_f32 v40, v40, s74, v223
	v_exp_f32_e32 v173, v173
	v_med3_f32 v41, v41, s74, v223
	v_pk_add_f32 v[166:167], v[166:167], 1.0 op_sel_hi:[1,0]
	v_pk_add_f32 v[168:169], v[168:169], 1.0 op_sel_hi:[1,0]
	v_pk_add_f32 v[170:171], v[170:171], 1.0 op_sel_hi:[1,0]
	v_pk_add_f32 v[172:173], v[172:173], 1.0 op_sel_hi:[1,0]
	v_rcp_f32_e32 v166, v166
	v_rcp_f32_e32 v167, v167
	v_pk_add_f32 v[46:47], v[46:47], 1.0 op_sel_hi:[1,0]
	v_rcp_f32_e32 v168, v168
	v_rcp_f32_e32 v169, v169
	v_pk_add_f32 v[48:49], v[48:49], 1.0 op_sel_hi:[1,0]
	v_rcp_f32_e32 v170, v170
	v_rcp_f32_e32 v171, v171
	v_pk_add_f32 v[38:39], v[38:39], 1.0 op_sel_hi:[1,0]
	v_rcp_f32_e32 v172, v172
	v_rcp_f32_e32 v173, v173
	v_pk_add_f32 v[40:41], v[40:41], 1.0 op_sel_hi:[1,0]
	s_nop 0
	v_pk_mul_f32 v[50:51], v[50:51], v[166:167]
	v_pk_mul_f32 v[52:53], v[52:53], v[168:169]
	v_pk_mul_f32 v[42:43], v[42:43], v[170:171]
	v_pk_mul_f32 v[44:45], v[44:45], v[172:173]
	v_pk_mul_f32 v[46:47], v[46:47], v[50:51]
	v_pk_mul_f32 v[48:49], v[48:49], v[52:53]
	v_pk_mul_f32 v[38:39], v[38:39], v[42:43]
	v_pk_mul_f32 v[40:41], v[40:41], v[44:45]
	v_pk_fma_f32 v[46:47], v[46:47], v[176:177], v[222:223] op_sel_hi:[1,0,0]
	v_pk_fma_f32 v[48:49], v[48:49], v[176:177], v[222:223] op_sel_hi:[1,0,0]
	v_pk_fma_f32 v[38:39], v[38:39], v[176:177], v[222:223] op_sel_hi:[1,0,0]
	v_pk_fma_f32 v[40:41], v[40:41], v[176:177], v[222:223] op_sel_hi:[1,0,0]
	v_med3_f32 v46, v46, s75, v224
	v_med3_f32 v47, v47, s75, v224
	v_med3_f32 v48, v48, s75, v224
	v_med3_f32 v49, v49, s75, v224
	v_med3_f32 v38, v38, s75, v224
	v_med3_f32 v39, v39, s75, v224
	v_med3_f32 v40, v40, s75, v224
	v_med3_f32 v41, v41, s75, v224
	v_perm_b32 v46, v47, v46, s76
	v_perm_b32 v48, v49, v48, s76
	v_perm_b32 v38, v39, v38, s76
	v_perm_b32 v40, v41, v40, s76
	v_perm_b32 v166, v48, v46, s77
	v_perm_b32 v167, v40, v38, s77
	v_add_u32_e32 v38, s4, v54
	v_ashrrev_i32_e32 v39, 31, v38
	v_lshlrev_b64 v[38:39], 11, v[38:39]
	v_lshl_add_u64 v[38:39], s[10:11], 0, v[38:39]
	v_lshl_add_u64 v[38:39], v[38:39], 0, v[4:5]
	v_mov_b32_e32 v46, v166
	v_mov_b32_e32 v47, v167
	global_store_dwordx2 v[38:39], v[46:47], off
.LBB0_977:
	s_or_b64 exec, exec, s[0:1]
	v_add_u32_e32 v38, 0xa0, v150
	v_cmp_lt_i32_e32 vcc, v38, v151
	s_and_saveexec_b64 s[0:1], vcc
	s_cbranch_execz .LBB0_979
	v_mul_f32_e32 v174, 0x3a800000, v152
	v_cvt_f32_i32_e32 v34, v34
	v_cvt_f32_i32_e32 v35, v35
	v_cvt_f32_i32_e32 v36, v36
	v_cvt_f32_i32_e32 v37, v37
	v_cvt_f32_i32_e32 v30, v30
	v_cvt_f32_i32_e32 v31, v31
	v_cvt_f32_i32_e32 v32, v32
	v_cvt_f32_i32_e32 v33, v33
	v_cvt_f32_i32_e32 v26, v26
	v_cvt_f32_i32_e32 v27, v27
	v_cvt_f32_i32_e32 v28, v28
	v_cvt_f32_i32_e32 v29, v29
	v_cvt_f32_i32_e32 v22, v22
	v_cvt_f32_i32_e32 v23, v23
	v_cvt_f32_i32_e32 v24, v24
	v_cvt_f32_i32_e32 v25, v25
	v_pk_fma_f32 v[34:35], v[34:35], v[174:175], v[146:147] op_sel_hi:[1,0,1]
	v_pk_fma_f32 v[30:31], v[30:31], v[174:175], v[142:143] op_sel_hi:[1,0,1]
	v_pk_fma_f32 v[36:37], v[36:37], v[174:175], v[148:149] op_sel_hi:[1,0,1]
	v_pk_fma_f32 v[32:33], v[32:33], v[174:175], v[144:145] op_sel_hi:[1,0,1]
	v_pk_fma_f32 v[26:27], v[26:27], v[174:175], v[130:131] op_sel_hi:[1,0,1]
	v_pk_fma_f32 v[22:23], v[22:23], v[174:175], v[126:127] op_sel_hi:[1,0,1]
	v_pk_fma_f32 v[28:29], v[28:29], v[174:175], v[132:133] op_sel_hi:[1,0,1]
	v_pk_fma_f32 v[24:25], v[24:25], v[174:175], v[128:129] op_sel_hi:[1,0,1]
	v_min_f32_e32 v34, 0x40e00000, v34
	v_min_f32_e32 v35, 0x40e00000, v35
	v_min_f32_e32 v36, 0x40e00000, v36
	v_min_f32_e32 v37, 0x40e00000, v37
	v_min_f32_e32 v26, 0x40e00000, v26
	v_min_f32_e32 v27, 0x40e00000, v27
	v_min_f32_e32 v28, 0x40e00000, v28
	v_min_f32_e32 v29, 0x40e00000, v29
	v_pk_mul_f32 v[166:167], v[34:35], v[178:179] op_sel_hi:[1,0]
	v_pk_mul_f32 v[168:169], v[36:37], v[178:179] op_sel_hi:[1,0]
	v_pk_mul_f32 v[170:171], v[26:27], v[178:179] op_sel_hi:[1,0]
	v_pk_mul_f32 v[172:173], v[28:29], v[178:179] op_sel_hi:[1,0]
	v_exp_f32_e32 v166, v166
	v_med3_f32 v30, v30, s74, v223
	v_exp_f32_e32 v167, v167
	v_med3_f32 v31, v31, s74, v223
	v_exp_f32_e32 v168, v168
	v_med3_f32 v32, v32, s74, v223
	v_exp_f32_e32 v169, v169
	v_med3_f32 v33, v33, s74, v223
	v_exp_f32_e32 v170, v170
	v_med3_f32 v22, v22, s74, v223
	v_exp_f32_e32 v171, v171
	v_med3_f32 v23, v23, s74, v223
	v_exp_f32_e32 v172, v172
	v_med3_f32 v24, v24, s74, v223
	v_exp_f32_e32 v173, v173
	v_med3_f32 v25, v25, s74, v223
	v_pk_add_f32 v[166:167], v[166:167], 1.0 op_sel_hi:[1,0]
	v_pk_add_f32 v[168:169], v[168:169], 1.0 op_sel_hi:[1,0]
	v_pk_add_f32 v[170:171], v[170:171], 1.0 op_sel_hi:[1,0]
	v_pk_add_f32 v[172:173], v[172:173], 1.0 op_sel_hi:[1,0]
	v_rcp_f32_e32 v166, v166
	v_rcp_f32_e32 v167, v167
	v_pk_add_f32 v[30:31], v[30:31], 1.0 op_sel_hi:[1,0]
	v_rcp_f32_e32 v168, v168
	v_rcp_f32_e32 v169, v169
	v_pk_add_f32 v[32:33], v[32:33], 1.0 op_sel_hi:[1,0]
	v_rcp_f32_e32 v170, v170
	v_rcp_f32_e32 v171, v171
	v_pk_add_f32 v[22:23], v[22:23], 1.0 op_sel_hi:[1,0]
	v_rcp_f32_e32 v172, v172
	v_rcp_f32_e32 v173, v173
	v_pk_add_f32 v[24:25], v[24:25], 1.0 op_sel_hi:[1,0]
	s_nop 0
	v_pk_mul_f32 v[34:35], v[34:35], v[166:167]
	v_pk_mul_f32 v[36:37], v[36:37], v[168:169]
	v_pk_mul_f32 v[26:27], v[26:27], v[170:171]
	v_pk_mul_f32 v[28:29], v[28:29], v[172:173]
	v_pk_mul_f32 v[30:31], v[30:31], v[34:35]
	v_pk_mul_f32 v[32:33], v[32:33], v[36:37]
	v_pk_mul_f32 v[22:23], v[22:23], v[26:27]
	v_pk_mul_f32 v[24:25], v[24:25], v[28:29]
	v_pk_fma_f32 v[30:31], v[30:31], v[176:177], v[222:223] op_sel_hi:[1,0,0]
	v_pk_fma_f32 v[32:33], v[32:33], v[176:177], v[222:223] op_sel_hi:[1,0,0]
	v_pk_fma_f32 v[22:23], v[22:23], v[176:177], v[222:223] op_sel_hi:[1,0,0]
	v_pk_fma_f32 v[24:25], v[24:25], v[176:177], v[222:223] op_sel_hi:[1,0,0]
	v_med3_f32 v30, v30, s75, v224
	v_med3_f32 v31, v31, s75, v224
	v_med3_f32 v32, v32, s75, v224
	v_med3_f32 v33, v33, s75, v224
	v_med3_f32 v22, v22, s75, v224
	v_med3_f32 v23, v23, s75, v224
	v_med3_f32 v24, v24, s75, v224
	v_med3_f32 v25, v25, s75, v224
	v_perm_b32 v30, v31, v30, s76
	v_perm_b32 v32, v33, v32, s76
	v_perm_b32 v22, v23, v22, s76
	v_perm_b32 v24, v25, v24, s76
	v_perm_b32 v166, v32, v30, s77
	v_perm_b32 v167, v24, v22, s77
	v_add_u32_e32 v22, s4, v38
	v_ashrrev_i32_e32 v23, 31, v22
	v_lshlrev_b64 v[22:23], 11, v[22:23]
	v_lshl_add_u64 v[22:23], s[10:11], 0, v[22:23]
	v_lshl_add_u64 v[22:23], v[22:23], 0, v[4:5]
	v_mov_b32_e32 v30, v166
	v_mov_b32_e32 v31, v167
	global_store_dwordx2 v[22:23], v[30:31], off
.LBB0_979:
	s_or_b64 exec, exec, s[0:1]
	v_add_u32_e32 v22, 0xb0, v150
	v_cmp_lt_i32_e32 vcc, v22, v151
	s_and_saveexec_b64 s[0:1], vcc
	s_cbranch_execz .LBB0_981
	v_mul_f32_e32 v174, 0x3a800000, v3
	v_cvt_f32_i32_e32 v18, v18
	v_cvt_f32_i32_e32 v19, v19
	v_cvt_f32_i32_e32 v20, v20
	v_cvt_f32_i32_e32 v21, v21
	v_cvt_f32_i32_e32 v14, v14
	v_cvt_f32_i32_e32 v15, v15
	v_cvt_f32_i32_e32 v16, v16
	v_cvt_f32_i32_e32 v17, v17
	v_cvt_f32_i32_e32 v10, v10
	v_cvt_f32_i32_e32 v11, v11
	v_cvt_f32_i32_e32 v12, v12
	v_cvt_f32_i32_e32 v13, v13
	v_cvt_f32_i32_e32 v6, v6
	v_cvt_f32_i32_e32 v7, v7
	v_cvt_f32_i32_e32 v8, v8
	v_cvt_f32_i32_e32 v9, v9
	v_pk_fma_f32 v[18:19], v[18:19], v[174:175], v[146:147] op_sel_hi:[1,0,1]
	v_pk_fma_f32 v[14:15], v[14:15], v[174:175], v[142:143] op_sel_hi:[1,0,1]
	v_pk_fma_f32 v[20:21], v[20:21], v[174:175], v[148:149] op_sel_hi:[1,0,1]
	v_pk_fma_f32 v[16:17], v[16:17], v[174:175], v[144:145] op_sel_hi:[1,0,1]
	v_pk_fma_f32 v[10:11], v[10:11], v[174:175], v[130:131] op_sel_hi:[1,0,1]
	v_pk_fma_f32 v[6:7], v[6:7], v[174:175], v[126:127] op_sel_hi:[1,0,1]
	v_pk_fma_f32 v[12:13], v[12:13], v[174:175], v[132:133] op_sel_hi:[1,0,1]
	v_pk_fma_f32 v[8:9], v[8:9], v[174:175], v[128:129] op_sel_hi:[1,0,1]
	v_min_f32_e32 v18, 0x40e00000, v18
	v_min_f32_e32 v19, 0x40e00000, v19
	v_min_f32_e32 v20, 0x40e00000, v20
	v_min_f32_e32 v21, 0x40e00000, v21
	v_min_f32_e32 v10, 0x40e00000, v10
	v_min_f32_e32 v11, 0x40e00000, v11
	v_min_f32_e32 v12, 0x40e00000, v12
	v_min_f32_e32 v13, 0x40e00000, v13
	v_pk_mul_f32 v[166:167], v[18:19], v[178:179] op_sel_hi:[1,0]
	v_pk_mul_f32 v[168:169], v[20:21], v[178:179] op_sel_hi:[1,0]
	v_pk_mul_f32 v[170:171], v[10:11], v[178:179] op_sel_hi:[1,0]
	v_pk_mul_f32 v[172:173], v[12:13], v[178:179] op_sel_hi:[1,0]
	v_exp_f32_e32 v166, v166
	v_med3_f32 v14, v14, s74, v223
	v_exp_f32_e32 v167, v167
	v_med3_f32 v15, v15, s74, v223
	v_exp_f32_e32 v168, v168
	v_med3_f32 v16, v16, s74, v223
	v_exp_f32_e32 v169, v169
	v_med3_f32 v17, v17, s74, v223
	v_exp_f32_e32 v170, v170
	v_med3_f32 v6, v6, s74, v223
	v_exp_f32_e32 v171, v171
	v_med3_f32 v7, v7, s74, v223
	v_exp_f32_e32 v172, v172
	v_med3_f32 v8, v8, s74, v223
	v_exp_f32_e32 v173, v173
	v_med3_f32 v9, v9, s74, v223
	v_pk_add_f32 v[166:167], v[166:167], 1.0 op_sel_hi:[1,0]
	v_pk_add_f32 v[168:169], v[168:169], 1.0 op_sel_hi:[1,0]
	v_pk_add_f32 v[170:171], v[170:171], 1.0 op_sel_hi:[1,0]
	v_pk_add_f32 v[172:173], v[172:173], 1.0 op_sel_hi:[1,0]
	v_rcp_f32_e32 v166, v166
	v_rcp_f32_e32 v167, v167
	v_pk_add_f32 v[14:15], v[14:15], 1.0 op_sel_hi:[1,0]
	v_rcp_f32_e32 v168, v168
	v_rcp_f32_e32 v169, v169
	v_pk_add_f32 v[16:17], v[16:17], 1.0 op_sel_hi:[1,0]
	v_rcp_f32_e32 v170, v170
	v_rcp_f32_e32 v171, v171
	v_pk_add_f32 v[6:7], v[6:7], 1.0 op_sel_hi:[1,0]
	v_rcp_f32_e32 v172, v172
	v_rcp_f32_e32 v173, v173
	v_pk_add_f32 v[8:9], v[8:9], 1.0 op_sel_hi:[1,0]
	s_nop 0
	v_pk_mul_f32 v[18:19], v[18:19], v[166:167]
	v_pk_mul_f32 v[20:21], v[20:21], v[168:169]
	v_pk_mul_f32 v[10:11], v[10:11], v[170:171]
	v_pk_mul_f32 v[12:13], v[12:13], v[172:173]
	v_pk_mul_f32 v[14:15], v[14:15], v[18:19]
	v_pk_mul_f32 v[16:17], v[16:17], v[20:21]
	v_pk_mul_f32 v[6:7], v[6:7], v[10:11]
	v_pk_mul_f32 v[8:9], v[8:9], v[12:13]
	v_pk_fma_f32 v[14:15], v[14:15], v[176:177], v[222:223] op_sel_hi:[1,0,0]
	v_pk_fma_f32 v[16:17], v[16:17], v[176:177], v[222:223] op_sel_hi:[1,0,0]
	v_pk_fma_f32 v[6:7], v[6:7], v[176:177], v[222:223] op_sel_hi:[1,0,0]
	v_pk_fma_f32 v[8:9], v[8:9], v[176:177], v[222:223] op_sel_hi:[1,0,0]
	v_med3_f32 v14, v14, s75, v224
	v_med3_f32 v15, v15, s75, v224
	v_med3_f32 v16, v16, s75, v224
	v_med3_f32 v17, v17, s75, v224
	v_med3_f32 v6, v6, s75, v224
	v_med3_f32 v7, v7, s75, v224
	v_med3_f32 v8, v8, s75, v224
	v_med3_f32 v9, v9, s75, v224
	v_perm_b32 v14, v15, v14, s76
	v_perm_b32 v16, v17, v16, s76
	v_perm_b32 v6, v7, v6, s76
	v_perm_b32 v8, v9, v8, s76
	v_perm_b32 v166, v16, v14, s77
	v_perm_b32 v167, v8, v6, s77
	v_add_u32_e32 v6, s4, v22
	v_ashrrev_i32_e32 v7, 31, v6
	v_lshlrev_b64 v[6:7], 11, v[6:7]
	v_lshl_add_u64 v[6:7], s[10:11], 0, v[6:7]
	v_lshl_add_u64 v[4:5], v[6:7], 0, v[4:5]
	v_mov_b32_e32 v14, v166
	v_mov_b32_e32 v15, v167
	global_store_dwordx2 v[4:5], v[14:15], off
